# P1 of layers 0-2 split in three classes: 128 WGs 3 GEMM units + 3 stolen tiles, 64 WGs 4 GEMM units (two virtual workgroups), 64 WGs convert 10 next-layer tiles for the whole phase; conversion tail af
# speedup vs baseline: 1.0095x; 1.0095x over previous
; #define LAS __attribute__((address_space(3)))
; template <class T> __device__ __forceinline__ T* opaque_p(T* p) { asm volatile("" : "+s"(p)); return p; }
; __device__ __forceinline__ int tidx(int wid) { int l; asm volatile("v_mbcnt_lo_u32_b32 %0, -1, 0\n\tv_mbcnt_hi_u32_b32 %0, -1, %0" : "=v"(l)); return (wid << 6) + l; }
; __device__ __forceinline__ int opaque_s(int v) { asm volatile("" : "+s"(v)); return v; }
; __global__ void __launch_bounds__(NTHREADS, 2) hybrid_fwd(Args a) {
;     ...
;     for (int l = 0; l < NLAYER; ++l) {
;         const int pb = 1 + l * NPH;
;         if (PHEN(1) && IN(pb + 0)) for (int rep = 0; rep < NREP(1); ++rep) { unsigned char* ws = opaque_p(a.ws); LAS unsigned char* lds = opaque_p(lds0); const int bid = opaque_s((int)blockIdx.x); const int tid = tidx(wid0), lane = tid & 63, wave = __builtin_amdgcn_readfirstlane(tid >> 6), gw = bid * NWAVES + wave; (void)lane; (void)gw;
;             pg8::Gemm g{ws, (unsigned)WS_XB, (unsigned)(WS_WIN + (size_t)l * DIN * DM), DM / 2, DM / 2, opaque_s(DM / 2)};
;             pg8::GridOrder S; S.init(MTOK, DIN, DM / 2, DM / 2, G, bid);
;             EpiZ E{(bf16_t*)(ws + WS_Z), (const float*)(ws + WS_COS), (const float*)(ws + WS_SIN)};
;             pg8::gemm_phase<EpiZ, pg8::GridOrder, true, true>(lds, g, S, E, wid0);
;             if (l + 1 < NLAYER && G == 256 && bid >= 128)
;                 f8_convert<true>(a, lds, ws, l + 1, 0, 0, 2, (unsigned*)(ws + WS_CTL) + CW_TICK + 64 * (l + 1), tid, lane, wave);
.LBB0_165:
	s_or_b64 exec, exec, s[2:3]
	s_load_dwordx4 s[4:7], s[0:1], 0xe0
	s_ashr_i32 s82, s81, 31
	s_cmpk_eq_i32 s81, 0x100
	s_cselect_b64 s[96:97], -1, 0
	s_lshl_b32 s0, s33, 6
	s_waitcnt lgkmcnt(0)
	v_writelane_b32 v255, s4, 6
	s_sub_i32 s86, 0, s0
	s_lshl_b32 s36, s81, 4
	v_writelane_b32 v255, s5, 7
	v_writelane_b32 v255, s6, 8
	v_writelane_b32 v255, s7, 9
	s_movk_i32 s83, 0x2000
	v_readlane_b32 s0, v255, 5
	s_lshl_b32 s91, s0, 6
	s_add_i32 s0, s81, 0xffffff80
	v_writelane_b32 v255, s0, 10
	s_ashr_i32 s0, s0, 31
	v_writelane_b32 v255, s0, 11
	s_lshl_b32 s0, s81, 1
	v_writelane_b32 v255, s0, 12
	s_and_b32 s0, s81, 7
	s_cmp_lg_u32 s0, 0
	s_cselect_b64 s[0:1], -1, 0
	v_writelane_b32 v255, s0, 13
	s_ashr_i32 s37, s36, 31
	s_lshl_b32 s94, s81, 5
	v_writelane_b32 v255, s1, 14
	s_ashr_i32 s0, s81, 3
	v_writelane_b32 v255, s0, 15
	s_lshl_b32 s0, s81, 6
	v_writelane_b32 v255, s0, 16
	s_add_i32 s0, 0, 0x20620
	v_writelane_b32 v255, s0, 17
	s_add_i32 s0, 0, 0x20624
	v_writelane_b32 v255, s0, 18
	s_lshl_b64 s[0:1], s[36:37], 11
	v_writelane_b32 v255, s0, 19
	s_mov_b32 s59, 0x20000
	s_brev_b32 s58, -2
	v_writelane_b32 v255, s1, 20
	s_lshl_b64 s[0:1], s[36:37], 13
	v_writelane_b32 v255, s0, 21
	s_mov_b32 s87, 0xa000
	s_mov_b32 s70, 0xc000
	v_writelane_b32 v255, s1, 22
	s_lshl_b64 s[0:1], s[36:37], 12
	v_writelane_b32 v255, s0, 23
	v_mov_b32_e32 v193, 0
	s_movk_i32 s85, 0x2800
	v_writelane_b32 v255, s1, 24
	v_writelane_b32 v255, s78, 25
	v_writelane_b32 v255, s79, 26
	v_writelane_b32 v255, s82, 27
	v_writelane_b32 v255, s96, 28
	v_mov_b32_e32 v206, 1
	s_movk_i32 s62, 0x5000
	v_writelane_b32 v255, s97, 29
	v_writelane_b32 v255, s86, 30
	v_writelane_b32 v255, s91, 31
	v_writelane_b32 v255, s94, 32
	v_writelane_b32 v255, s60, 33
	s_mov_b32 s69, 0xc3e00000
	s_movk_i32 s33, 0x1000
	v_writelane_b32 v255, s61, 34
	v_writelane_b32 v255, s36, 35
	s_mov_b32 s89, 0xff800000
	s_brev_b32 s68, -3
	s_mov_b32 s52, 0x41000000
	s_movk_i32 s63, 0x7000
	s_mov_b32 s76, 0xf000
	v_mov_b32_e32 v207, 0x3727c5ac
	v_mov_b32_e32 v208, 0x43e00000
	v_mov_b32_e32 v209, 8
	v_mov_b32_e32 v210, 0xff800000
	v_mov_b32_e32 v211, 0xd800
	v_mov_b32_e32 v241, 0x7f800000
	v_mov_b32_e32 v254, 0x50000
	v_mov_b32_e32 v214, 0x2800
	v_mov_b64_e32 v[212:213], 0x100
	s_mov_b32 s80, 0x3d000000
	s_mov_b32 s84, 0x3e0293ee
	s_mov_b32 s88, 0x3b800000
	s_mov_b32 s90, 0x3fd744fd
	s_mov_b32 s72, 0x3d800000
	s_mov_b32 s66, s93
	v_writelane_b32 v255, s37, 36
	v_writelane_b32 v255, 0, 61
	s_branch .LBB0_169

; #define LAS __attribute__((address_space(3)))
; template <class T> __device__ __forceinline__ T* opaque_p(T* p) { asm volatile("" : "+s"(p)); return p; }
; __device__ __forceinline__ int tidx(int wid) { int l; asm volatile("v_mbcnt_lo_u32_b32 %0, -1, 0\n\tv_mbcnt_hi_u32_b32 %0, -1, %0" : "=v"(l)); return (wid << 6) + l; }
; __device__ __forceinline__ int opaque_s(int v) { asm volatile("" : "+s"(v)); return v; }
;     __device__ bool next(int i, Unit& u) const {
;         const long L = (long)i * G + c; if (L >= nwg) return false;
;         int wgid = (int)L; { const int q = nwg / NXCD, r = nwg % NXCD, xcd = wgid % NXCD, off = wgid / NXCD; wgid = (xcd < r ? xcd * (q + 1) : r * (q + 1) + (xcd - r) * q) + off; }
;         const int nig = WGM * nN, gid = wgid / nig, fm = gid * WGM, gsz = (nM - fm) < WGM ? (nM - fm) : WGM;
;         u.pm = fm + ((wgid % nig) % gsz); u.pn = (wgid % nig) / gsz; u.aoff = (unsigned)u.pm * atile; u.boff = (unsigned)u.pn * btile; return true;
; __global__ void __launch_bounds__(NTHREADS, 2) hybrid_fwd(Args a) {
;     ...
;         if (PHEN(1) && IN(pb + 0)) for (int rep = 0; rep < NREP(1); ++rep) { unsigned char* ws = opaque_p(a.ws); LAS unsigned char* lds = opaque_p(lds0); const int bid = opaque_s((int)blockIdx.x); const int tid = tidx(wid0), lane = tid & 63, wave = __builtin_amdgcn_readfirstlane(tid >> 6), gw = bid * NWAVES + wave; (void)lane; (void)gw;
;             pg8::Gemm g{ws, (unsigned)WS_XB, (unsigned)(WS_WIN + (size_t)l * DIN * DM), DM / 2, DM / 2, opaque_s(DM / 2)};
;             pg8::GridOrder S; S.init(MTOK, DIN, DM / 2, DM / 2, G, bid);
;             EpiZ E{(bf16_t*)(ws + WS_Z), (const float*)(ws + WS_COS), (const float*)(ws + WS_SIN)};
;             pg8::gemm_phase<EpiZ, pg8::GridOrder, true, true>(lds, g, S, E, wid0);
.Lcg_setup:
	v_readlane_b32 s0, v255, 6
	v_readlane_b32 s2, v255, 8
	v_readlane_b32 s3, v255, 9
	s_mov_b64 s[4:5], s[2:3]
	s_mov_b32 s26, s93
	v_readlane_b32 s21, v255, 0
	v_readlane_b32 s6, v255, 61
	s_nop 0
	s_cmp_eq_u32 s6, 1
	s_cbranch_scc0 .Lcg_a
	s_addk_i32 s21, 0x40
.Lcg_a:
	s_movk_i32 s2, 0x400
	v_readlane_b32 s1, v255, 7
	v_mbcnt_lo_u32_b32 v172, -1, 0
	v_mbcnt_hi_u32_b32 v172, -1, v172
	s_waitcnt vmcnt(0)
	v_mbcnt_lo_u32_b32 v0, -1, 0
	v_mbcnt_hi_u32_b32 v0, -1, v0
	s_cmpk_lt_i32 s21, 0x280
	v_add_u32_e32 v173, s78, v172
	v_add_u32_e32 v1, s78, v0
	v_readfirstlane_b32 s20, v173
	s_cselect_b64 s[0:1], -1, 0
	v_readlane_b32 s6, v255, 61
	s_nop 0
	s_cmp_lg_u32 s6, 0
	s_cbranch_scc1 .Lcg_nodiv
	s_cmpk_lt_i32 s21, 0xc0
	s_cbranch_scc1 .Lcg_nodiv
	s_cmp_eq_u32 s66, 3
	s_cbranch_scc1 .Lcg_nodiv
	v_writelane_b32 v255, 3, 61
	s_branch .LBB0_208
.Lcg_nodiv:
	s_cmpk_gt_i32 s21, 0x27f
	v_readfirstlane_b32 s3, v1
	s_cbranch_scc1 .LBB0_174
	s_ashr_i32 s6, s21, 31
	s_lshr_b32 s6, s6, 29
	s_add_i32 s6, s21, s6
	s_ashr_i32 s7, s6, 3
	s_and_b32 s6, s6, -8
	s_sub_i32 s6, s21, s6
	s_cmp_lt_i32 s6, 0
	s_movk_i32 s8, 0x51
	s_cselect_b32 s8, s8, 0x50
	s_mul_i32 s6, s6, s8
	s_add_i32 s6, s6, s7
	s_mul_hi_i32 s7, s6, 0x66666667
	s_lshr_b32 s8, s7, 31
	s_ashr_i32 s7, s7, 6
	s_add_i32 s7, s7, s8
	s_lshl_b32 s8, s7, 3
	s_mulk_i32 s7, 0xa0
	s_sub_i32 s6, s6, s7
	s_bfe_u32 s7, s6, 0x3001c
	s_add_i32 s7, s6, s7
	s_sext_i32_i16 s9, s7
	s_and_b32 s7, s7, 0xfff8
	s_sub_i32 s6, s6, s7
	s_sext_i32_i16 s6, s6
	s_add_i32 s18, s8, s6
	s_ashr_i32 s55, s9, 3
	s_lshl_b32 s10, s18, 19
	s_lshl_b32 s6, s55, 19

; #define LAS __attribute__((address_space(3)))
; template <bool STEAL>
; __device__ __forceinline__ void f8_convert(const Args& a, LAS unsigned char* lds, unsigned char* ws, int l, int first, int stride, int quota, unsigned* ticket, int tid, int lane, int wave) {
;     volatile LAS int* word = (volatile LAS int*)(lds + MISC_OFF) + 16;
;     f32x4 v[32];
;     int k, n = 0;
;     if constexpr (STEAL) {
;         __syncthreads();
;         if (first != -2) {
;             if (tid == 0) word[0] = (quota > 0) ? (int)__hip_atomic_fetch_add(ticket, 1u, __ATOMIC_RELAXED, __HIP_MEMORY_SCOPE_AGENT) : F8_TILES_PER_LAYER;
;             __syncthreads(); }
; __global__ void __launch_bounds__(NTHREADS, 2) hybrid_fwd(Args a) {
;     ...
;             if (l + 1 < NLAYER && G == 256 && bid >= 128)
;                 f8_convert<true>(a, lds, ws, l + 1, 0, 0, 2, (unsigned*)(ws + WS_CTL) + CW_TICK + 64 * (l + 1), tid, lane, wave);
.LBB0_208:
	v_readlane_b32 s0, v255, 61
	s_nop 0
	s_cmp_eq_u32 s0, 1
	s_cbranch_scc1 .Lcg_skipc
	s_cmp_eq_u32 s0, 3
	s_cbranch_scc1 .Lcg_208
	s_cmp_eq_u32 s66, 3
	s_cbranch_scc1 .Lcg_208
	s_cmpk_gt_i32 s21, 0x7f
	s_cbranch_scc1 .Lcg_skipc
	s_movk_i32 s21, 0x100
	s_branch .Lcg_208
.Lcg_skipc:
	s_branch .LBB0_284
.Lcg_208:
	s_cmp_lg_u32 s66, 3
	s_cselect_b64 s[0:1], -1, 0
	s_cmpk_gt_i32 s21, 0x7f
	s_cselect_b64 s[2:3], -1, 0
	s_and_b64 s[0:1], s[0:1], s[2:3]
	s_and_b64 s[0:1], s[0:1], s[96:97]
	s_andn2_b64 vcc, exec, s[0:1]
	s_cbranch_vccnz .LBB0_284
	s_add_i32 s31, s66, 1
	s_lshl_b32 s92, s31, 6
	s_lshl_b64 s[0:1], s[92:93], 2
	s_add_u32 s0, s4, s0
	s_addc_u32 s1, s5, s1
	s_add_u32 s6, s0, 0x9000
	s_addc_u32 s7, s1, 0
	s_add_i32 s27, s26, 0x20640
	v_cmp_ne_u32_e64 s[0:1], 0, v173
	v_cmp_eq_u32_e32 vcc, 0, v173
	s_waitcnt vmcnt(0) lgkmcnt(0)
	s_barrier
	s_and_saveexec_b64 s[2:3], vcc
	s_cbranch_execz .LBB0_211
	v_mov_b64_e32 v[0:1], s[6:7]
	flat_atomic_add v0, v[0:1], v206 sc0
	v_mov_b32_e32 v1, s27
	s_waitcnt vmcnt(0) lgkmcnt(0)
	ds_write_b32 v1, v0

; #define LAS __attribute__((address_space(3)))
; template <bool STEAL>
; __device__ __forceinline__ void f8_convert(const Args& a, LAS unsigned char* lds, unsigned char* ws, int l, int first, int stride, int quota, unsigned* ticket, int tid, int lane, int wave) {
;     ...
;     while (k < F8_TILES_PER_LAYER) {
;         LAS unsigned char* buf = lds + (n & 1) * 65536;
;         if constexpr (STEAL) { if (tid == 0) word[(n + 1) & 1] = (n + 1 < quota) ? (int)__hip_atomic_fetch_add(ticket, 1u, __ATOMIC_RELAXED, __HIP_MEMORY_SCOPE_AGENT) : F8_TILES_PER_LAYER; }
.LBB0_247:
	s_and_saveexec_b64 s[2:3], s[0:1]
	s_xor_b64 s[2:3], exec, s[2:3]
	s_and_b32 s4, s35, 1
	s_or_saveexec_b64 s[2:3], s[2:3]
	v_mov_b32_e32 v152, s4
	s_xor_b64 exec, exec, s[2:3]
	s_cbranch_execz .LBB0_253
	v_readlane_b32 s4, v255, 61
	s_nop 0
	s_cmp_eq_u32 s4, 3
	s_cselect_b32 s4, 9, 2
	s_cmp_gt_u32 s35, s4
	v_mov_b32_e32 v152, 0x6e0
	s_cbranch_scc1 .LBB0_252
	v_mov_b64_e32 v[152:153], s[6:7]
	flat_atomic_add v152, v[152:153], v206 sc0

; #define LAS __attribute__((address_space(3)))
; template <class T> __device__ __forceinline__ T* opaque_p(T* p) { asm volatile("" : "+s"(p)); return p; }
; __device__ __forceinline__ int tidx(int wid) { int l; asm volatile("v_mbcnt_lo_u32_b32 %0, -1, 0\n\tv_mbcnt_hi_u32_b32 %0, -1, %0" : "=v"(l)); return (wid << 6) + l; }
; __device__ __forceinline__ int opaque_s(int v) { asm volatile("" : "+s"(v)); return v; }
; __global__ void __launch_bounds__(NTHREADS, 2) hybrid_fwd(Args a) {
;     ...
;         if (PHEN(1) && IN(pb + 0)) for (int rep = 0; rep < NREP(1); ++rep) { unsigned char* ws = opaque_p(a.ws); LAS unsigned char* lds = opaque_p(lds0); const int bid = opaque_s((int)blockIdx.x); const int tid = tidx(wid0), lane = tid & 63, wave = __builtin_amdgcn_readfirstlane(tid >> 6), gw = bid * NWAVES + wave; (void)lane; (void)gw;
;             pg8::Gemm g{ws, (unsigned)WS_XB, (unsigned)(WS_WIN + (size_t)l * DIN * DM), DM / 2, DM / 2, opaque_s(DM / 2)};
;             pg8::GridOrder S; S.init(MTOK, DIN, DM / 2, DM / 2, G, bid);
;             EpiZ E{(bf16_t*)(ws + WS_Z), (const float*)(ws + WS_COS), (const float*)(ws + WS_SIN)};
;             pg8::gemm_phase<EpiZ, pg8::GridOrder, true, true>(lds, g, S, E, wid0);
;             if (l + 1 < NLAYER && G == 256 && bid >= 128)
;                 f8_convert<true>(a, lds, ws, l + 1, 0, 0, 2, (unsigned*)(ws + WS_CTL) + CW_TICK + 64 * (l + 1), tid, lane, wave);
;         }
.LBB0_284:
	v_readlane_b32 s36, v255, 61
	s_nop 0
	s_cmp_eq_u32 s36, 0
	s_cbranch_scc1 .Lcg_first
	v_writelane_b32 v255, 0, 61
	s_branch .Lcg_x
.Lcg_first:
	v_readlane_b32 s36, v255, 0
	s_nop 0
	s_cmpk_lt_i32 s36, 0x80
	s_cbranch_scc1 .Lcg_x
	s_cmpk_gt_i32 s36, 0xbf
	s_cbranch_scc1 .Lcg_x
	s_cmp_eq_u32 s66, 3
	s_cbranch_scc1 .Lcg_x
	v_writelane_b32 v255, 1, 61
	s_waitcnt vmcnt(0) lgkmcnt(0)
	s_barrier
	s_branch .Lcg_setup
